# attention unit prologue: first QK^T K-fragment reads batched; N2 router B fragments kept in registers for the phase (on top of DPP softmax + nt hints)
# baseline (speedup 1.0000x reference)
; #define WAIT_BAR(N) asm volatile("s_waitcnt vmcnt(" #N ") lgkmcnt(0)\n\ts_barrier":::"memory")
;   #define DMA_K(t,slot) glds16(ksrc+(long)TILE(t)*(KVBLK*KVPT),(unsigned)__builtin_amdgcn_readfirstlane(kdst+(slot)))
;   #define DMA_V(t,slot) glds16(vsrc+(long)TILE(t)*(KVBLK*KVPT),(unsigned)__builtin_amdgcn_readfirstlane(vdst+(slot)))
;   #define CMASK(P0,P1,t) do{int jb_=(t)-(NT-nband); if(jb_>=0)wmask(P0,P1,krel0+64*jb_,qrel,hi,wq);}while(0)
;   #define CMASK(P0,P1,t) do{}while(0)
;   #define CMASK(P0,P1,t) do{int jb_=(t)-(NT-nband); if(jb_>=0)wmask(P0,P1,krel0+64*jb_,qrel,hi,wq);}while(0)
; template<int THRL> __device__ __forceinline__ void attn_unit(const AttU&U,const bf16*Q,const bf16*__restrict__ K,const bf16*__restrict__ V,bf16*O,char*shm){
;   int tid_=threadIdx.x; asm volatile("":"+v"(tid_)); const int tid=tid_,lane=tid&63,r32=lane&31,hi=lane>>5; const int wid=__builtin_amdgcn_readfirstlane(tid>>6);
;   const int NT=U.NT,nA=U.nA,tA=U.tA,tB=U.tB,nband=U.nband,krel0=U.krel0;
;   const int wq=wid&U.wqm, wh=wid>>U.whs;
;   const bf16*Qw=Q+((long)U.qrow0+wq*QBLK)*DM+U.qcol+wh*D;
;   const bf16*Kh=K+(long)U.kvrow0*KVPT+U.kvcol,*Vh=V+(long)U.kvrow0*KVPT+U.kvcol;
;   const unsigned lds0=(unsigned)(uintptr_t)shm;
;   float*wsf=(float*)(shm+LDS_WS)+wid*64;
;   const bf16*ksrc=Kh+(long)lane*KVPT+wid*8;
;   const bf16*vsrc=Vh+(long)(16*(wid&3)+(lane>>2))*KVPT+(wid>>2)*32+(lane&3)*8;
;   const unsigned kdst=lds0+LDS_K+wid*1024, vdst=lds0+LDS_V+wid*1024;
;     ...
;   const int vb0=(int)(lds0+LDS_V)+((lane>>4)&1)*32+(lane&3)*8+(4*hi+((lane&15)>>2))*64;
;   const char*Kbase=shm+LDS_K; bf16x8 kf[8];
;   const lds_cptr shm3=(lds_cptr)shm; const lds_cptr kp0=shm3+LDS_K+hi*1024+r32*16; const lds_cptr vp0=shm3+LDS_V+((lane>>4)&1)*32+(lane&3)*8+(4*hi+((lane&15)>>2))*64;
;   DMA_K(0,0);DMA_V(0,0);DMA_K(1,SLOTB);
;   bf16x8 qr[4];
;   #pragma unroll
;   for(int d0=0;d0<4;++d0)qr[d0]=*reinterpret_cast<const bf16x8*>(&Qw[(long)r32*DM+d0*16+hi*8]);
;   float mhat=0.f,l_reg=0.f;f32x16 o[2];o[0]=f32x16{};o[1]=f32x16{};f32x16 negm=f32x16{};asm volatile("":"+v"(negm));
;   const int qrel=wq*QBLK+r32;
;     ...
;   bool resc=false;
;     ...
;   f32x16 pA0,pA1,pB0,pB1;
;   int sl_prev=0,sl_cur=0,sl_next=SLOTB;
;     ...
;   DMA_K(2,2*SLOTB);
;   WAIT_BAR(3);
;   qkt(pA0,pA1,Kbase,qr,negm,r32,hi);asm volatile("s_nop 15\n\ts_nop 7":"+v"(pA0),"+v"(pA1));CMASK(pA0,pA1,0);
.LBB0_911:
	v_mov_b32_e32 v34, v0
	s_ashr_i32 s3, s1, 31
	v_readfirstlane_b32 s6, v34
	s_ashr_i32 s17, s6, 6
	s_and_b32 s2, s17, s9
	s_ashr_i32 s18, s17, s18
	s_lshl_b32 s23, s2, 5
	s_add_u32 s40, s23, s1
	s_addc_u32 s41, 0, s3
	s_lshl_b64 s[2:3], s[40:41], 11
	v_readlane_b32 s8, v252, 13
	v_readlane_b32 s9, v252, 14
	s_add_u32 s1, s8, s2
	s_addc_u32 s8, s9, s3
	s_lshl_b64 s[2:3], s[12:13], 1
	s_add_u32 s1, s1, s2
	s_addc_u32 s8, s8, s3
	s_lshl_b32 s38, s18, 6
	s_ashr_i32 s39, s38, 31
	s_lshl_b64 s[2:3], s[38:39], 1
	s_add_u32 s2, s1, s2
	s_addc_u32 s3, s8, s3
	s_mul_i32 s7, s7, 0x120000
	v_readlane_b32 s8, v253, 32
	v_readlane_b32 s9, v253, 33
	s_add_u32 s8, s8, s7
	s_mov_b32 s1, s13
	s_addc_u32 s9, s9, 0
	s_lshl_b64 s[0:1], s[0:1], 1
	s_add_u32 s8, s8, s0
	s_addc_u32 s9, s9, s1
	v_readlane_b32 s30, v253, 49
	v_readlane_b32 s31, v253, 50
	s_add_u32 s7, s30, s7
	v_and_b32_e32 v199, 63, v34
	s_addc_u32 s25, s31, 0
	s_add_u32 s0, s7, s0
	v_lshlrev_b32_e32 v190, 9, v199
	s_addc_u32 s1, s25, s1
	v_lshl_add_u64 v[2:3], s[8:9], 0, v[190:191]
	s_lshl_b32 s8, s17, 3
	s_ashr_i32 s9, s8, 31
	s_lshl_b32 s7, s17, 4
	v_bfe_u32 v193, v34, 2, 4
	v_lshl_add_u64 v[194:195], s[8:9], 1, v[2:3]
	v_and_or_b32 v2, s7, 48, v193
	v_lshlrev_b32_e32 v190, 9, v2
	v_lshl_add_u64 v[2:3], s[0:1], 0, v[190:191]
	s_ashr_i32 s0, s6, 3
	s_andn2_b32 s0, s0, 31
	s_ashr_i32 s1, s0, 31
	s_lshl_b32 s30, s17, 10
	s_cmp_lg_u32 0, -1
	v_lshl_add_u64 v[2:3], s[0:1], 1, v[2:3]
	v_and_b32_e32 v35, 3, v34
	s_cselect_b32 s0, 0, 0
	v_lshlrev_b32_e32 v190, 4, v35
	s_add_i32 s30, s30, s0
	s_lshl_b32 s0, s29, 15
	s_mov_b32 s1, s13
	v_lshl_add_u64 v[196:197], v[2:3], 0, v[190:191]
	v_lshl_add_u64 v[82:83], v[194:195], 0, s[0:1]
	s_mov_b32 s7, m0
	s_mov_b32 m0, s30
	s_nop 0
	global_load_lds_dwordx4 v[82:83], off
	s_mov_b32 m0, s7
	s_add_i32 s31, s30, 0x6000
	v_lshl_add_u64 v[2:3], v[196:197], 0, s[0:1]
	s_mov_b32 s1, m0
	s_mov_b32 m0, s31
	s_nop 0
	global_load_lds_dwordx4 v[2:3], off
	s_mov_b32 m0, s1
	s_bitset1_b32 s0, 15
	s_mov_b32 s1, s13
	v_and_b32_e32 v198, 31, v34
	v_lshl_add_u64 v[2:3], v[194:195], 0, s[0:1]
	v_bfe_u32 v206, v34, 5, 1
	s_add_i32 s7, s30, 0x2000
	s_mov_b32 s8, m0
	s_mov_b32 m0, s7
	s_nop 0
	global_load_lds_dwordx4 v[2:3], off
	s_mov_b32 m0, s8
	v_lshlrev_b32_e32 v2, 11, v198
	v_lshl_or_b32 v16, v206, 4, v2
	global_load_dwordx4 v[138:141], v16, s[2:3]
	global_load_dwordx4 v[130:133], v16, s[2:3] offset:32
	global_load_dwordx4 v[118:121], v16, s[2:3] offset:64
	global_load_dwordx4 v[114:117], v16, s[2:3] offset:96
	v_mov_b32_e32 v2, v191
	v_mov_b32_e32 v3, v191
	v_mov_b32_e32 v4, v191
	v_mov_b32_e32 v5, v191
	v_mov_b32_e32 v6, v191
	v_mov_b32_e32 v7, v191
	v_mov_b32_e32 v8, v191
	v_mov_b32_e32 v9, v191
	v_mov_b32_e32 v10, v191
	v_mov_b32_e32 v11, v191
	v_mov_b32_e32 v12, v191
	v_mov_b32_e32 v13, v191
	v_mov_b32_e32 v14, v191
	v_mov_b32_e32 v15, v191
	v_mov_b32_e32 v16, v191
	v_mov_b32_e32 v17, v191
	v_lshlrev_b32_e32 v18, 10, v206
	v_lshlrev_b32_e32 v19, 4, v198
	s_mov_b64 s[2:3], 0x10000
	v_add3_u32 v214, 0, v18, v19
	v_lshl_add_u64 v[18:19], v[82:83], 0, s[2:3]
	s_add_i32 s2, s30, 0x4000
	s_mov_b32 s3, m0
	s_mov_b32 m0, s2
	s_nop 0
	global_load_lds_dwordx4 v[18:19], off
	s_mov_b32 m0, s3
	s_waitcnt vmcnt(3) lgkmcnt(0)
	s_barrier
	ds_read_b128 v[174:177], v214
	ds_read_b128 v[170:173], v214 offset:512
	ds_read_b128 v[166:169], v214 offset:2048
	ds_read_b128 v[162:165], v214 offset:2560
	ds_read_b128 v[158:161], v214 offset:4096
	ds_read_b128 v[154:157], v214 offset:4608
	ds_read_b128 v[150:153], v214 offset:6144
	ds_read_b128 v[146:149], v214 offset:6656
	s_sub_i32 s25, s22, s4
	v_or_b32_e32 v207, s23, v198
	s_cmp_gt_i32 s25, 0
	s_waitcnt vmcnt(3) lgkmcnt(6)
	v_mfma_f32_32x32x16_bf16 v[18:33], v[174:177], v[138:141], v[2:17]
	v_mfma_f32_32x32x16_bf16 v[2:17], v[170:173], v[138:141], v[2:17]
	s_waitcnt vmcnt(2) lgkmcnt(4)
	v_mfma_f32_32x32x16_bf16 v[18:33], v[166:169], v[130:133], v[18:33]
	v_mfma_f32_32x32x16_bf16 v[2:17], v[162:165], v[130:133], v[2:17]
	s_waitcnt vmcnt(1) lgkmcnt(2)
	v_mfma_f32_32x32x16_bf16 v[18:33], v[158:161], v[118:121], v[18:33]
	v_mfma_f32_32x32x16_bf16 v[2:17], v[154:157], v[118:121], v[2:17]
	s_waitcnt vmcnt(0) lgkmcnt(0)
	v_mfma_f32_32x32x16_bf16 v[18:33], v[150:153], v[114:117], v[18:33]
	v_mfma_f32_32x32x16_bf16 v[2:17], v[146:149], v[114:117], v[2:17]
	s_nop 15
	s_nop 7
	s_cbranch_scc1 .LBB0_914
; __device__ __forceinline__ void wmask(f32x16&p0,f32x16&p1,int krel,int qrel,int hi,int wid){
;   const int dlo=krel-(32*wid+31), dhi=krel+63-32*wid;
;   if(dlo>=-128&&dhi<=128)return;
;   float xf=(float)(krel+4*hi-qrel); asm volatile("":"+v"(xf));
;   #pragma unroll
;   for(int r=0;r<16;++r){const float c=(float)((r&3)+8*(r>>2));
;     p0[r]=__builtin_fmaf(__builtin_fminf(128.f-__builtin_fabsf(xf+c),0.f),1e30f,p0[r]);
;     p1[r]=__builtin_fmaf(__builtin_fminf(128.f-__builtin_fabsf(xf+(c+32.f)),0.f),1e30f,p1[r]);}
; }
	s_lshl_b32 s2, s25, 6
	s_sub_i32 s2, s19, s2
	s_sub_i32 s3, s2, s23
	s_addk_i32 s3, 0x61
	s_cmpk_lt_u32 s3, 0xa3
	s_cbranch_scc1 .LBB0_914
	v_lshl_or_b32 v36, v206, 2, s2
	v_sub_u32_e32 v36, v36, v207
	v_cvt_f32_i32_e32 v67, v36
	s_nop 0
	v_add_f32_e32 v37, 0x42000000, v67
	v_add_f32_e32 v39, 1.0, v67
	v_sub_f32_e64 v37, s27, |v37|
	v_sub_f32_e64 v36, s27, |v67|
	v_min_f32_e32 v38, 0, v37
	v_sub_f32_e64 v37, s27, |v39|
	v_add_f32_e32 v41, 0x42080000, v67
	v_add_f32_e32 v45, 0x42200000, v67
	v_add_f32_e32 v49, 0x42280000, v67
	v_add_f32_e32 v53, 0x42400000, v67
	v_add_f32_e32 v57, 0x42480000, v67
	v_add_f32_e32 v61, 0x42600000, v67
	v_add_f32_e32 v65, 0x42680000, v67
	v_min_f32_e32 v36, 0, v36
	v_min_f32_e32 v37, 0, v37
	v_sub_f32_e64 v41, s27, |v41|
	v_sub_f32_e64 v45, s27, |v45|
	v_sub_f32_e64 v49, s27, |v49|
	v_sub_f32_e64 v53, s27, |v53|
	v_sub_f32_e64 v57, s27, |v57|
	v_sub_f32_e64 v61, s27, |v61|
	v_sub_f32_e64 v65, s27, |v65|
	v_add_f32_e32 v39, 0x42040000, v67
	v_add_f32_e32 v40, 2.0, v67
	v_min_f32_e32 v42, 0, v41
	v_add_f32_e32 v41, 0x40400000, v67
	v_add_f32_e32 v43, 0x420c0000, v67
	v_add_f32_e32 v44, 0x41000000, v67
	v_min_f32_e32 v46, 0, v45
	v_add_f32_e32 v45, 0x41100000, v67
	v_add_f32_e32 v47, 0x42240000, v67
	v_add_f32_e32 v48, 0x41200000, v67
	v_min_f32_e32 v50, 0, v49
	v_add_f32_e32 v49, 0x41300000, v67
	v_add_f32_e32 v51, 0x422c0000, v67
	v_add_f32_e32 v52, 0x41800000, v67
	v_min_f32_e32 v54, 0, v53
	v_add_f32_e32 v53, 0x41880000, v67
	v_add_f32_e32 v55, 0x42440000, v67
	v_add_f32_e32 v56, 0x41900000, v67
	v_min_f32_e32 v58, 0, v57
	v_add_f32_e32 v57, 0x41980000, v67
	v_add_f32_e32 v59, 0x424c0000, v67
	v_add_f32_e32 v60, 0x41c00000, v67
	v_min_f32_e32 v62, 0, v61
	v_add_f32_e32 v61, 0x41c80000, v67
	v_add_f32_e32 v63, 0x42640000, v67
	v_add_f32_e32 v64, 0x41d00000, v67
	v_min_f32_e32 v66, 0, v65
	v_add_f32_e32 v65, 0x41d80000, v67
	v_pk_fma_f32 v[18:19], v[36:37], s[20:21], v[18:19] op_sel_hi:[1,0,1]
	v_add_f32_e32 v36, 0x426c0000, v67
	v_sub_f32_e64 v39, s27, |v39|
	v_sub_f32_e64 v40, s27, |v40|
	v_sub_f32_e64 v41, s27, |v41|
	v_sub_f32_e64 v43, s27, |v43|
	v_sub_f32_e64 v44, s27, |v44|
	v_sub_f32_e64 v45, s27, |v45|
	v_sub_f32_e64 v47, s27, |v47|
	v_sub_f32_e64 v48, s27, |v48|
	v_sub_f32_e64 v49, s27, |v49|
	v_sub_f32_e64 v51, s27, |v51|
	v_sub_f32_e64 v52, s27, |v52|
	v_sub_f32_e64 v53, s27, |v53|
	v_sub_f32_e64 v55, s27, |v55|
	v_sub_f32_e64 v56, s27, |v56|
	v_sub_f32_e64 v57, s27, |v57|
	v_sub_f32_e64 v59, s27, |v59|
	v_sub_f32_e64 v60, s27, |v60|
	v_sub_f32_e64 v61, s27, |v61|
	v_sub_f32_e64 v63, s27, |v63|
	v_sub_f32_e64 v64, s27, |v64|
	v_sub_f32_e64 v65, s27, |v65|
	v_sub_f32_e64 v36, s27, |v36|
	v_min_f32_e32 v39, 0, v39
	v_min_f32_e32 v40, 0, v40
	v_min_f32_e32 v41, 0, v41
	v_min_f32_e32 v43, 0, v43
	v_min_f32_e32 v44, 0, v44
	v_min_f32_e32 v45, 0, v45
	v_min_f32_e32 v47, 0, v47
	v_min_f32_e32 v48, 0, v48
	v_min_f32_e32 v49, 0, v49
	v_min_f32_e32 v51, 0, v51
	v_min_f32_e32 v52, 0, v52
	v_min_f32_e32 v53, 0, v53
	v_min_f32_e32 v55, 0, v55
	v_min_f32_e32 v56, 0, v56
	v_min_f32_e32 v57, 0, v57
	v_min_f32_e32 v59, 0, v59
	v_min_f32_e32 v60, 0, v60
	v_min_f32_e32 v61, 0, v61
	v_min_f32_e32 v63, 0, v63
	v_min_f32_e32 v64, 0, v64
	v_min_f32_e32 v65, 0, v65
	v_min_f32_e32 v67, 0, v36
	v_pk_fma_f32 v[32:33], v[64:65], s[20:21], v[32:33] op_sel_hi:[1,0,1]
	v_pk_fma_f32 v[30:31], v[60:61], s[20:21], v[30:31] op_sel_hi:[1,0,1]
	v_pk_fma_f32 v[28:29], v[56:57], s[20:21], v[28:29] op_sel_hi:[1,0,1]
	v_pk_fma_f32 v[26:27], v[52:53], s[20:21], v[26:27] op_sel_hi:[1,0,1]
	v_pk_fma_f32 v[24:25], v[48:49], s[20:21], v[24:25] op_sel_hi:[1,0,1]
	v_pk_fma_f32 v[22:23], v[44:45], s[20:21], v[22:23] op_sel_hi:[1,0,1]
	v_pk_fma_f32 v[20:21], v[40:41], s[20:21], v[20:21] op_sel_hi:[1,0,1]
	v_pk_fma_f32 v[16:17], v[66:67], s[20:21], v[16:17] op_sel_hi:[1,0,1]
	v_pk_fma_f32 v[14:15], v[62:63], s[20:21], v[14:15] op_sel_hi:[1,0,1]
	v_pk_fma_f32 v[12:13], v[58:59], s[20:21], v[12:13] op_sel_hi:[1,0,1]
	v_pk_fma_f32 v[10:11], v[54:55], s[20:21], v[10:11] op_sel_hi:[1,0,1]
	v_pk_fma_f32 v[8:9], v[50:51], s[20:21], v[8:9] op_sel_hi:[1,0,1]
	v_pk_fma_f32 v[6:7], v[46:47], s[20:21], v[6:7] op_sel_hi:[1,0,1]
	v_pk_fma_f32 v[4:5], v[42:43], s[20:21], v[4:5] op_sel_hi:[1,0,1]
	v_pk_fma_f32 v[2:3], v[38:39], s[20:21], v[2:3] op_sel_hi:[1,0,1]

; #define GAS __attribute__((address_space(1)))
; #define LAS __attribute__((address_space(3)))
; __device__ __forceinline__ void n2_phase(const Frame& F0, int L, int nrows) {
;     ...
;     { const GAS u32x4* img = (const GAS u32x4*)(F.ws + WS_RIMG + (size_t)L * 65536) + F.tid;
;       u32x4 iv[8];
; #pragma unroll
;       for (int i = 0; i < 8; ++i) iv[i] = img[512 * i];
; #pragma unroll
;       for (int i = 0; i < 8; ++i) *((LAS u32x4*)WH + F.tid + 512 * i) = iv[i]; }
;     __syncthreads();
;     const float* gn = inp(F, I_N2G) + L * 1024; const float* modL = (const float*)(F.ws + WS_MOD) + (size_t)L * 17 * 6144;
;     unsigned char* H8 = F.ws + WS_H; float* AFF = (float*)(F.ws + WS_AFF); const bf16_t* X = (const bf16_t*)(F.ws + WS_X);
;     const int RPB = nrows / F.G, NG = RPB / 16, rb = (int)blockIdx.x * RPB;
;     const int r = F.lane & 15, kg = F.lane >> 4, c0 = 128 * F.wave + 8 * kg;
;     u32x4 nraw[4];
; #pragma unroll
;     for (int s_ = 0; s_ < 4; ++s_) nraw[s_] = *(const GAS u32x4*)(X + (size_t)(rb + r) * D + c0 + 32 * s_);
;     f32x4 gs[4][2], sh[4][2];
;     ...
;         for (int s_ = 0; s_ < 4; ++s_) { const int o = ((16 * F.wave + 4 * s_ + kg) * 16 + r) * 8;
;             const bf16x8 bh = *(const LAS bf16x8*)(WH + o), bl = *(const LAS bf16x8*)(WL + o);
.LBB0_1200:
	s_andn2_b64 vcc, exec, s[0:1]
	s_cbranch_vccnz .LBB0_1268
	v_readlane_b32 s0, v255, 17
	v_readlane_b32 s1, v255, 18
	s_lshl_b64 s[0:1], s[0:1], 16
	v_readlane_b32 s2, v254, 5
	s_waitcnt vmcnt(0) lgkmcnt(0)
	v_mov_b32_e32 v18, v0
	s_add_u32 s0, s2, s0
	v_readlane_b32 s2, v254, 6
	s_addc_u32 s1, s2, s1
	v_ashrrev_i32_e32 v19, 31, v18
	v_lshl_add_u64 v[28:29], v[18:19], 4, s[0:1]
	s_movk_i32 s0, 0x2000
	v_add_co_u32_e32 v6, vcc, s0, v28
	s_movk_i32 s0, 0x4000
	s_nop 0
	v_addc_co_u32_e32 v7, vcc, 0, v29, vcc
	v_add_co_u32_e32 v10, vcc, s0, v28
	s_movk_i32 s0, 0x6000
	s_nop 0
	v_addc_co_u32_e32 v11, vcc, 0, v29, vcc
	v_add_co_u32_e32 v14, vcc, s0, v28
	s_mov_b32 s0, 0x8000
	s_nop 0
	v_addc_co_u32_e32 v15, vcc, 0, v29, vcc
	v_add_co_u32_e32 v20, vcc, s0, v28
	s_mov_b32 s0, 0xa000
	s_nop 0
	v_addc_co_u32_e32 v21, vcc, 0, v29, vcc
	v_add_co_u32_e32 v24, vcc, s0, v28
	s_mov_b32 s0, 0xc000
	s_nop 0
	v_addc_co_u32_e32 v25, vcc, 0, v29, vcc
	v_add_co_u32_e32 v30, vcc, s0, v28
	s_mov_b32 s0, 0xe000
	s_nop 0
	v_addc_co_u32_e32 v31, vcc, 0, v29, vcc
	v_add_co_u32_e32 v32, vcc, s0, v28
	global_load_dwordx4 v[2:5], v[28:29], off
	s_nop 0
	global_load_dwordx4 v[6:9], v[6:7], off
	v_addc_co_u32_e32 v33, vcc, 0, v29, vcc
	global_load_dwordx4 v[10:13], v[10:11], off
	s_nop 0
	global_load_dwordx4 v[14:17], v[14:15], off
	s_nop 0
	global_load_dwordx4 v[20:23], v[20:21], off
	s_nop 0
	global_load_dwordx4 v[24:27], v[24:25], off
	s_nop 0
	global_load_dwordx4 v[28:31], v[30:31], off
	s_nop 0
	global_load_dwordx4 v[32:35], v[32:33], off
	v_readlane_b32 s0, v255, 10
	v_readlane_b32 s3, v255, 16
	v_readlane_b32 s5, v254, 60
	v_mov_b32_e32 v1, s0
	v_readlane_b32 s0, v254, 61
	s_mul_hi_u32 s1, s3, s0
	s_mul_i32 s2, s1, s5
	s_sub_i32 s2, s3, s2
	s_add_i32 s3, s1, 1
	s_sub_i32 s4, s2, s5
	s_cmp_ge_u32 s2, s5
	v_lshl_add_u32 v19, v18, 4, 0
	s_cselect_b32 s1, s3, s1
	s_cselect_b32 s2, s4, s2
	s_add_i32 s3, s1, 1
	s_cmp_ge_u32 s2, s5
	s_cselect_b32 s1, s3, s1
	v_readlane_b32 s2, v252, 10
	s_xor_b32 s1, s1, s2
	s_sub_i32 s3, s1, s2
	v_readfirstlane_b32 s0, v18
	s_cmp_lt_i32 s3, 16
	s_waitcnt vmcnt(7)
	ds_write_b128 v19, v[2:5]
	s_waitcnt vmcnt(3)
	ds_write_b128 v19, v[20:23] offset:32768
	ds_write_b128 v19, v[6:9] offset:8192
	ds_write_b128 v19, v[10:13] offset:16384
	ds_write_b128 v19, v[14:17] offset:24576
	s_waitcnt vmcnt(2)
	ds_write_b128 v19, v[24:27] offset:40960
	s_waitcnt vmcnt(1)
	ds_write_b128 v19, v[28:31] offset:49152
	s_waitcnt vmcnt(0)
	ds_write_b128 v19, v[32:35] offset:57344
	s_waitcnt lgkmcnt(0)
	s_barrier
	ds_read_b64 v[2:3], v1
	s_waitcnt lgkmcnt(0)
	v_readfirstlane_b32 s1, v2
	v_readfirstlane_b32 s2, v3
	s_cbranch_scc1 .LBB0_1214
	s_mul_i32 s4, s3, s84
	v_and_b32_e32 v26, 15, v18
	v_bfe_u32 v27, v18, 4, 2
	s_ashr_i32 s8, s0, 6
	v_lshlrev_b32_e32 v1, 3, v27
	v_add_u32_e32 v82, s4, v26
	v_lshl_or_b32 v20, s8, 7, v1
	v_ashrrev_i32_e32 v83, 31, v82
	v_readlane_b32 s10, v252, 20
	v_ashrrev_i32_e32 v21, 31, v20
	v_lshlrev_b64 v[2:3], 11, v[82:83]
	v_readlane_b32 s11, v252, 21
	v_lshlrev_b64 v[22:23], 1, v[20:21]
	s_ashr_i32 s5, s3, 31
	v_lshl_add_u64 v[2:3], s[10:11], 0, v[2:3]
	v_lshl_add_u64 v[2:3], v[2:3], 0, v[22:23]
	global_load_dwordx4 v[14:17], v[2:3], off offset:192 nt
	global_load_dwordx4 v[10:13], v[2:3], off offset:128 nt
	global_load_dwordx4 v[6:9], v[2:3], off offset:64 nt
	s_nop 0
	global_load_dwordx4 v[2:5], v[2:3], off nt
	s_lshr_b32 s5, s5, 28
	v_readlane_b32 s6, v255, 17
	s_add_i32 s3, s3, s5
	v_readlane_b32 s7, v255, 18
	s_lshl_b32 s12, s6, 10
	s_ashr_i32 s5, s3, 4
	s_lshl_b64 s[6:7], s[12:13], 2
	s_add_u32 s6, s1, s6
	s_addc_u32 s7, s2, s7
	s_add_i32 s1, 0, 0x10000
	v_lshlrev_b32_e32 v190, 2, v26
	s_andn2_b32 s0, s0, 63
	v_and_b32_e32 v18, 63, v18
	v_add_u32_e32 v1, s1, v190
	s_add_i32 s0, s0, s1
	v_lshlrev_b32_e32 v28, 8, v27
	v_readlane_b32 s1, v255, 11
	v_lshl_add_u64 v[84:85], s[10:11], 0, v[22:23]
	v_cmp_gt_u32_e64 s[36:37], 16, v18
	v_lshl_add_u32 v83, v18, 2, s0
	v_add_u32_e32 v29, s1, v190
	v_cmp_gt_u32_e64 s[38:39], 32, v18
	s_lshl_b32 s1, s8, 1
	v_readlane_b32 s2, v254, 7
	v_or_b32_e32 v18, 32, v20
	v_or_b32_e32 v22, 64, v20
	v_or_b32_e32 v24, 0x60, v20
	v_lshl_or_b32 v31, s8, 12, v28
	s_lshl_b32 s0, s8, 10
	v_add_u32_e32 v30, s1, v27
	v_readlane_b32 s3, v254, 8
	v_ashrrev_i32_e32 v19, 31, v18
	v_or_b32_e32 v92, 36, v20
	v_ashrrev_i32_e32 v23, 31, v22
	v_or_b32_e32 v94, 0x44, v20
	v_ashrrev_i32_e32 v25, 31, v24
	v_or_b32_e32 v96, 0x64, v20
	v_lshl_or_b32 v26, v26, 4, v31
	s_add_i32 s1, s1, s4
	v_lshl_add_u64 v[86:87], s[96:97], 0, v[20:21]
	v_lshl_add_u64 v[88:89], s[2:3], 0, v[190:191]
	v_lshl_add_u64 v[90:91], v[20:21], 2, s[6:7]
	v_ashrrev_i32_e32 v93, 31, v92
	v_ashrrev_i32_e32 v95, 31, v94
	v_ashrrev_i32_e32 v97, 31, v96
	v_add_u32_e32 v143, 0, v26
	ds_read_b128 v[214:217], v143
	ds_read_b128 v[218:221], v143 offset:32768
	ds_read_b128 v[222:225], v143 offset:1024
	ds_read_b128 v[226:229], v143 offset:33792
	ds_read_b128 v[230:233], v143 offset:2048
	ds_read_b128 v[234:237], v143 offset:34816
	ds_read_b128 v[238:241], v143 offset:3072
	ds_read_b128 v[242:245], v143 offset:35840
	v_lshl_add_u32 v156, v30, 6, v29
	v_add3_u32 v157, v29, s0, v28
	v_add_u32_e32 v158, s1, v27
	s_mov_b32 s7, 0
	v_lshlrev_b64 v[98:99], 2, v[20:21]
	v_lshlrev_b64 v[100:101], 2, v[18:19]
	v_lshlrev_b64 v[102:103], 2, v[22:23]
	v_lshlrev_b64 v[104:105], 2, v[24:25]
	s_branch .LBB0_1204

; #define GAS __attribute__((address_space(1)))
; __device__ __forceinline__ unsigned pk2(float lo, float hi) { unsigned r; asm("v_cvt_pk_bf16_f32 %0, %1, %2" : "=v"(r) : "v"(lo), "v"(hi)); return r; }
; __device__ __forceinline__ void n2_phase(const Frame& F0, int L, int nrows) {
;     ...
;         __syncthreads();
;         float tot = 0.f;
; #pragma unroll
;         for (int w = 0; w < 8; ++w) tot += PSS[(par * 8 + w) * 16 + r];
;         const float rinv = __builtin_amdgcn_rsqf(tot * (1.0f / D) + EPS);
;         u32x4 ahi[4], alo[4];
; #pragma unroll
;         for (int s_ = 0; s_ < 4; ++s_) {
;             const f32x4 h0 = (v[s_][0] * rinv) * gs[s_][0] + sh[s_][0], h1 = (v[s_][1] * rinv) * gs[s_][1] + sh[s_][1];
;             u32x4 hi; hi.x = pk2(h0[0], h0[1]); hi.y = pk2(h0[2], h0[3]); hi.z = pk2(h1[0], h1[1]); hi.w = pk2(h1[2], h1[3]);
;             { u32x2 h8; h8.x = pg8::pack4_fp8(h0[0] * pg8::SC_H2, h0[1] * pg8::SC_H2, h0[2] * pg8::SC_H2, h0[3] * pg8::SC_H2); h8.y = pg8::pack4_fp8(h1[0] * pg8::SC_H2, h1[1] * pg8::SC_H2, h1[2] * pg8::SC_H2, h1[3] * pg8::SC_H2);
;               *(GAS u32x2*)(H8 + (size_t)row * D + c0 + 32 * s_) = h8; } ahi[s_] = hi;
;             alo[s_].x = pk2(h0[0] - bf_lo(hi.x), h0[1] - bf_hi(hi.x)); alo[s_].y = pk2(h0[2] - bf_lo(hi.y), h0[3] - bf_hi(hi.y));
;             alo[s_].z = pk2(h1[0] - bf_lo(hi.z), h1[1] - bf_hi(hi.z)); alo[s_].w = pk2(h1[2] - bf_lo(hi.w), h1[3] - bf_hi(hi.w)); }
.LBB0_1210:
	s_or_b64 exec, exec, s[0:1]
	v_add_u32_e32 v52, s7, v1
	s_waitcnt lgkmcnt(0)
	s_barrier
	ds_read2_b32 v[50:51], v52 offset1:16
	v_ashrrev_i32_e32 v141, 31, v140
	s_lshl_b32 s3, s3, 13
	s_waitcnt lgkmcnt(0)
	v_add_f32_e32 v50, 0, v50
	v_add_f32_e32 v53, v50, v51
	ds_read2_b32 v[50:51], v52 offset0:32 offset1:48
	s_waitcnt lgkmcnt(0)
	v_add_f32_e32 v50, v53, v50
	v_add_f32_e32 v53, v50, v51
	ds_read2_b32 v[50:51], v52 offset0:64 offset1:80
	s_waitcnt lgkmcnt(0)
	v_add_f32_e32 v50, v53, v50
	v_add_f32_e32 v53, v50, v51
	ds_read2_b32 v[50:51], v52 offset0:96 offset1:112
	s_waitcnt lgkmcnt(0)
	v_add_f32_e32 v50, v53, v50
	v_add_f32_e32 v50, v50, v51
	v_fmamk_f32 v50, v50, 0x3a800000, v250
	v_rsq_f32_e32 v142, v50
	v_lshlrev_b64 v[50:51], 10, v[140:141]
	v_lshl_add_u64 v[140:141], v[86:87], 0, v[50:51]
	v_pk_mul_f32 v[50:51], v[142:143], v[154:155] op_sel_hi:[0,1]
	v_pk_fma_f32 v[56:57], v[108:109], v[50:51], v[22:23]
	v_pk_mul_f32 v[50:51], v[142:143], v[150:151] op_sel_hi:[0,1]
	v_mul_f32_e32 v58, 0x41000000, v56
	v_mul_f32_e32 v59, 0x41000000, v57
	v_med3_f32 v151, v58, s15, v212
	v_med3_f32 v59, v59, s15, v212
	v_mov_b32_e32 v58, 0
	v_pk_mul_f32 v[52:53], v[142:143], v[152:153] op_sel_hi:[0,1]
	v_cvt_pk_fp8_f32 v58, v151, v59
	v_pk_fma_f32 v[54:55], v[106:107], v[52:53], v[24:25]
	v_pk_fma_f32 v[60:61], v[112:113], v[50:51], v[18:19]
	v_mul_f32_e32 v139, 0x41000000, v54
	v_mul_f32_e32 v150, 0x41000000, v55
	v_med3_f32 v59, v139, s15, v212
	v_med3_f32 v139, v150, s15, v212
	v_cvt_pk_fp8_f32 v58, v59, v139 op_sel:[0,0,1]
	v_mul_f32_e32 v59, 0x41000000, v60
	v_mul_f32_e32 v139, 0x41000000, v61
	v_med3_f32 v152, v59, s15, v212
	v_med3_f32 v139, v139, s15, v212
	v_mov_b32_e32 v59, 0
	v_pk_mul_f32 v[52:53], v[142:143], v[148:149] op_sel_hi:[0,1]
	v_cvt_pk_fp8_f32 v59, v152, v139
	v_pk_fma_f32 v[148:149], v[110:111], v[52:53], v[20:21]
	v_cvt_pk_bf16_f32 v50, v56, v57
	v_cvt_pk_bf16_f32 v51, v54, v55
	v_cvt_pk_bf16_f32 v52, v60, v61
	v_pk_mul_f32 v[76:77], v[142:143], v[76:77] op_sel_hi:[0,1]
	v_mul_f32_e32 v150, 0x41000000, v148
	v_mul_f32_e32 v151, 0x41000000, v149
	v_med3_f32 v139, v150, s15, v212
	v_med3_f32 v150, v151, s15, v212
	v_cvt_pk_fp8_f32 v59, v139, v150 op_sel:[0,0,1]
	v_cvt_pk_bf16_f32 v53, v148, v149
	v_pk_mul_f32 v[74:75], v[142:143], v[74:75] op_sel_hi:[0,1]
	v_pk_mul_f32 v[68:69], v[142:143], v[68:69] op_sel_hi:[0,1]
	global_store_dwordx2 v[140:141], v[58:59], off
	v_lshlrev_b32_e32 v58, 16, v50
	v_sub_f32_e32 v56, v56, v58
	v_and_b32_e32 v58, 0xffff0000, v50
	v_sub_f32_e32 v57, v57, v58
	v_cvt_pk_bf16_f32 v58, v56, v57
	v_lshlrev_b32_e32 v56, 16, v51
	v_sub_f32_e32 v54, v54, v56
	v_and_b32_e32 v56, 0xffff0000, v51
	v_sub_f32_e32 v55, v55, v56
	v_cvt_pk_bf16_f32 v59, v54, v55
	v_lshlrev_b32_e32 v54, 16, v52
	v_and_b32_e32 v55, 0xffff0000, v52
	v_sub_f32_e32 v54, v60, v54
	v_sub_f32_e32 v55, v61, v55
	v_cvt_pk_bf16_f32 v60, v54, v55
	v_lshlrev_b32_e32 v54, 16, v53
	v_and_b32_e32 v55, 0xffff0000, v53
	v_sub_f32_e32 v54, v148, v54
	v_sub_f32_e32 v55, v149, v55
	v_cvt_pk_bf16_f32 v61, v54, v55
	v_pk_mul_f32 v[54:55], v[142:143], v[146:147] op_sel_hi:[0,1]
	v_pk_mul_f32 v[56:57], v[142:143], v[144:145] op_sel_hi:[0,1]
	v_pk_fma_f32 v[146:147], v[116:117], v[54:55], v[30:31]
	v_pk_fma_f32 v[144:145], v[114:115], v[56:57], v[32:33]
	v_pk_mul_f32 v[56:57], v[142:143], v[62:63] op_sel_hi:[0,1]
	v_mul_f32_e32 v62, 0x41000000, v146
	v_mul_f32_e32 v63, 0x41000000, v147
	v_med3_f32 v151, v62, s15, v212
	v_med3_f32 v63, v63, s15, v212
	v_mov_b32_e32 v62, 0
	v_cvt_pk_fp8_f32 v62, v151, v63
	v_pk_mul_f32 v[54:55], v[142:143], v[64:65] op_sel_hi:[0,1]
	v_mul_f32_e32 v139, 0x41000000, v144
	v_mul_f32_e32 v150, 0x41000000, v145
	v_pk_fma_f32 v[64:65], v[120:121], v[54:55], v[26:27]
	v_med3_f32 v63, v139, s15, v212
	v_med3_f32 v139, v150, s15, v212
	v_cvt_pk_fp8_f32 v62, v63, v139 op_sel:[0,0,1]
	v_mul_f32_e32 v63, 0x41000000, v64
	v_mul_f32_e32 v139, 0x41000000, v65
	v_med3_f32 v152, v63, s15, v212
	v_med3_f32 v139, v139, s15, v212
	v_mov_b32_e32 v63, 0
	v_cvt_pk_fp8_f32 v63, v152, v139
	v_pk_fma_f32 v[148:149], v[118:119], v[56:57], v[28:29]
	v_cvt_pk_bf16_f32 v54, v146, v147
	v_cvt_pk_bf16_f32 v55, v144, v145
	v_cvt_pk_bf16_f32 v56, v64, v65
	v_pk_mul_f32 v[66:67], v[142:143], v[66:67] op_sel_hi:[0,1]
	v_mul_f32_e32 v150, 0x41000000, v148
	v_mul_f32_e32 v151, 0x41000000, v149
	v_med3_f32 v139, v150, s15, v212
	v_med3_f32 v150, v151, s15, v212
	v_cvt_pk_fp8_f32 v63, v139, v150 op_sel:[0,0,1]
	v_and_b32_e32 v139, 0xffff0000, v55
	v_sub_f32_e32 v139, v145, v139
	v_cvt_pk_bf16_f32 v57, v148, v149
	global_store_dwordx2 v[140:141], v[62:63], off offset:32
	v_lshlrev_b32_e32 v62, 16, v54
	v_and_b32_e32 v63, 0xffff0000, v54
	v_sub_f32_e32 v62, v146, v62
	v_sub_f32_e32 v63, v147, v63
	v_cvt_pk_bf16_f32 v62, v62, v63
	v_lshlrev_b32_e32 v63, 16, v55
	v_sub_f32_e32 v63, v144, v63
	v_cvt_pk_bf16_f32 v63, v63, v139
	v_lshlrev_b32_e32 v139, 16, v56
	v_sub_f32_e32 v64, v64, v139
	v_and_b32_e32 v139, 0xffff0000, v56
	v_sub_f32_e32 v65, v65, v139
	v_cvt_pk_bf16_f32 v64, v64, v65
	v_lshlrev_b32_e32 v65, 16, v57
	v_and_b32_e32 v139, 0xffff0000, v57
	v_sub_f32_e32 v65, v148, v65
	v_sub_f32_e32 v139, v149, v139
	v_pk_fma_f32 v[144:145], v[122:123], v[74:75], v[40:41]
	v_pk_fma_f32 v[74:75], v[124:125], v[76:77], v[38:39]
	v_cvt_pk_bf16_f32 v65, v65, v139
	v_mul_f32_e32 v149, 0x41000000, v144
	v_mul_f32_e32 v139, 0x41000000, v74
	v_mul_f32_e32 v148, 0x41000000, v75
	v_med3_f32 v139, v139, s15, v212
	v_med3_f32 v151, v148, s15, v212
	v_mov_b32_e32 v148, 0
	v_cvt_pk_fp8_f32 v148, v139, v151
	v_mul_f32_e32 v150, 0x41000000, v145
; #define LAS __attribute__((address_space(3)))
; __device__ __forceinline__ void n2_phase(const Frame& F0, int L, int nrows) {
;     ...
;         f32x4 acc = (f32x4){0.f, 0.f, 0.f, 0.f};
; #pragma unroll
;         for (int s_ = 0; s_ < 4; ++s_) { const int o = ((16 * F.wave + 4 * s_ + kg) * 16 + r) * 8;
;             const bf16x8 bh = *(const LAS bf16x8*)(WH + o), bl = *(const LAS bf16x8*)(WL + o);
;             const bf16x8 ah = __builtin_bit_cast(bf16x8, ahi[s_]), al = __builtin_bit_cast(bf16x8, alo[s_]);
;             acc = __builtin_amdgcn_mfma_f32_16x16x32_bf16(ah, bh, acc, 0, 0, 0);
;             acc = __builtin_amdgcn_mfma_f32_16x16x32_bf16(ah, bl, acc, 0, 0, 0);
;             acc = __builtin_amdgcn_mfma_f32_16x16x32_bf16(al, bh, acc, 0, 0, 0); }
; #pragma unroll
;         for (int i = 0; i < 4; ++i) PLG[((par * 8 + F.wave) * 16 + 4 * kg + i) * 16 + r] = acc[i];
;         __syncthreads();
;         if (F.lane < 32) { const int rl = 2 * F.wave + (F.lane >> 4), e = F.lane & 15; float lg = 0.f;
; #pragma unroll
;             for (int w = 0; w < 8; ++w) lg += PLG[((par * 8 + w) * 16 + rl) * 16 + e];
;             float mx = lg;
; #pragma unroll
;             for (int o = 1; o < 16; o <<= 1) mx = fmaxf(mx, __shfl_xor(mx, o));
;             const float ex = __expf(lg - mx); float den = ex;
; #pragma unroll
;             for (int o = 1; o < 16; o <<= 1) den += __shfl_xor(den, o);
;             AFF[(size_t)(row0 + rl) * 16 + e] = ex / den; }
	v_pk_fma_f32 v[76:77], v[128:129], v[68:69], v[34:35]
	v_med3_f32 v139, v149, s15, v212
	v_med3_f32 v149, v150, s15, v212
	v_cvt_pk_fp8_f32 v148, v139, v149 op_sel:[0,0,1]
	v_mul_f32_e32 v139, 0x41000000, v76
	v_mul_f32_e32 v149, 0x41000000, v77
	v_med3_f32 v139, v139, s15, v212
	v_med3_f32 v152, v149, s15, v212
	v_mov_b32_e32 v149, 0
	v_cvt_pk_fp8_f32 v149, v139, v152
	v_pk_fma_f32 v[146:147], v[126:127], v[66:67], v[36:37]
	v_cvt_pk_bf16_f32 v66, v74, v75
	v_cvt_pk_bf16_f32 v67, v144, v145
	v_cvt_pk_bf16_f32 v68, v76, v77
	v_pk_mul_f32 v[80:81], v[142:143], v[80:81] op_sel_hi:[0,1]
	v_mul_f32_e32 v150, 0x41000000, v146
	v_mul_f32_e32 v151, 0x41000000, v147
	v_med3_f32 v139, v150, s15, v212
	v_med3_f32 v150, v151, s15, v212
	v_cvt_pk_fp8_f32 v149, v139, v150 op_sel:[0,0,1]
	v_lshlrev_b32_e32 v139, 16, v66
	v_sub_f32_e32 v74, v74, v139
	v_and_b32_e32 v139, 0xffff0000, v66
	v_sub_f32_e32 v75, v75, v139
	v_cvt_pk_bf16_f32 v74, v74, v75
	v_lshlrev_b32_e32 v75, 16, v67
	v_and_b32_e32 v139, 0xffff0000, v67
	v_sub_f32_e32 v75, v144, v75
	v_sub_f32_e32 v139, v145, v139
	v_cvt_pk_bf16_f32 v75, v75, v139
	v_lshlrev_b32_e32 v139, 16, v68
	v_sub_f32_e32 v76, v76, v139
	v_and_b32_e32 v139, 0xffff0000, v68
	v_sub_f32_e32 v77, v77, v139
	v_cvt_pk_bf16_f32 v69, v146, v147
	v_cvt_pk_bf16_f32 v76, v76, v77
	v_pk_mul_f32 v[78:79], v[142:143], v[78:79] op_sel_hi:[0,1]
	v_lshlrev_b32_e32 v77, 16, v69
	v_and_b32_e32 v139, 0xffff0000, v69
	v_sub_f32_e32 v77, v146, v77
	v_sub_f32_e32 v139, v147, v139
	v_pk_fma_f32 v[144:145], v[130:131], v[78:79], v[48:49]
	v_pk_fma_f32 v[78:79], v[132:133], v[80:81], v[46:47]
	v_cvt_pk_bf16_f32 v77, v77, v139
	v_pk_mul_f32 v[72:73], v[142:143], v[72:73] op_sel_hi:[0,1]
	v_pk_mul_f32 v[70:71], v[142:143], v[70:71] op_sel_hi:[0,1]
	v_mul_f32_e32 v139, 0x41000000, v78
	v_mul_f32_e32 v142, 0x41000000, v79
	global_store_dwordx2 v[140:141], v[148:149], off offset:64
	v_med3_f32 v139, v139, s15, v212
	v_med3_f32 v142, v142, s15, v212
	v_mov_b32_e32 v148, 0
	v_cvt_pk_fp8_f32 v148, v139, v142
	v_mul_f32_e32 v149, 0x41000000, v144
	v_mul_f32_e32 v150, 0x41000000, v145
	v_pk_fma_f32 v[80:81], v[136:137], v[72:73], v[42:43]
	v_med3_f32 v139, v149, s15, v212
	v_med3_f32 v142, v150, s15, v212
	v_cvt_pk_fp8_f32 v148, v139, v142 op_sel:[0,0,1]
	v_mul_f32_e32 v139, 0x41000000, v80
	v_mul_f32_e32 v142, 0x41000000, v81
	v_med3_f32 v139, v139, s15, v212
	v_med3_f32 v142, v142, s15, v212
	v_mov_b32_e32 v149, 0
	v_cvt_pk_fp8_f32 v149, v139, v142
	v_pk_fma_f32 v[146:147], v[134:135], v[70:71], v[44:45]
	v_cvt_pk_bf16_f32 v70, v78, v79
	v_cvt_pk_bf16_f32 v71, v144, v145
	v_cvt_pk_bf16_f32 v72, v80, v81
	s_nop 0
	v_mul_f32_e32 v150, 0x41000000, v146
	v_mul_f32_e32 v151, 0x41000000, v147
	v_med3_f32 v139, v150, s15, v212
	v_med3_f32 v142, v151, s15, v212
	v_cvt_pk_fp8_f32 v149, v139, v142 op_sel:[0,0,1]
	v_lshlrev_b32_e32 v139, 16, v70
	v_sub_f32_e32 v78, v78, v139
	v_and_b32_e32 v139, 0xffff0000, v70
	v_sub_f32_e32 v79, v79, v139
	v_cvt_pk_bf16_f32 v78, v78, v79
	v_lshlrev_b32_e32 v79, 16, v71
	v_and_b32_e32 v139, 0xffff0000, v71
	v_sub_f32_e32 v79, v144, v79
	v_sub_f32_e32 v139, v145, v139
	v_cvt_pk_bf16_f32 v79, v79, v139
	v_lshlrev_b32_e32 v139, 16, v72
	v_sub_f32_e32 v80, v80, v139
	v_and_b32_e32 v139, 0xffff0000, v72
	v_sub_f32_e32 v81, v81, v139
	v_cvt_pk_bf16_f32 v73, v146, v147
	global_store_dwordx2 v[140:141], v[148:149], off offset:96
	v_cvt_pk_bf16_f32 v80, v80, v81
	v_lshlrev_b32_e32 v81, 16, v73
	v_and_b32_e32 v139, 0xffff0000, v73
	v_sub_f32_e32 v81, v146, v81
	v_sub_f32_e32 v139, v147, v139
	v_mfma_f32_16x16x32_bf16 v[152:155], v[50:53], v[214:217], 0
	v_cvt_pk_bf16_f32 v81, v81, v139
	v_mfma_f32_16x16x32_bf16 v[50:53], v[50:53], v[218:221], v[152:155]
	v_mfma_f32_16x16x32_bf16 v[50:53], v[58:61], v[214:217], v[50:53]
	v_mfma_f32_16x16x32_bf16 v[50:53], v[54:57], v[222:225], v[50:53]
	v_mfma_f32_16x16x32_bf16 v[50:53], v[54:57], v[226:229], v[50:53]
	v_mfma_f32_16x16x32_bf16 v[50:53], v[62:65], v[222:225], v[50:53]
	v_mfma_f32_16x16x32_bf16 v[50:53], v[66:69], v[230:233], v[50:53]
	v_mfma_f32_16x16x32_bf16 v[50:53], v[66:69], v[234:237], v[50:53]
	v_mfma_f32_16x16x32_bf16 v[50:53], v[74:77], v[230:233], v[50:53]
	v_mfma_f32_16x16x32_bf16 v[50:53], v[70:73], v[238:241], v[50:53]
	v_mfma_f32_16x16x32_bf16 v[50:53], v[70:73], v[242:245], v[50:53]
	v_mfma_f32_16x16x32_bf16 v[50:53], v[78:81], v[238:241], v[50:53]
	v_add_u32_e32 v54, s3, v157
	s_nop 6
	ds_write2_b32 v54, v50, v51 offset1:16
	ds_write2_b32 v54, v52, v53 offset0:32 offset1:48
	s_waitcnt lgkmcnt(0)
	s_barrier
	s_and_saveexec_b64 s[0:1], s[38:39]
	s_cbranch_execz .LBB0_1212
	v_add_u32_e32 v52, s3, v156
	ds_read2st64_b32 v[50:51], v52 offset1:4
	ds_read2st64_b32 v[54:55], v52 offset0:8 offset1:12
	ds_read2st64_b32 v[56:57], v52 offset0:16 offset1:20
	ds_read2st64_b32 v[58:59], v52 offset0:24 offset1:28
	v_ashrrev_i32_e32 v139, 31, v138
	s_waitcnt lgkmcnt(0)
	v_add_f32_e32 v50, 0, v50
	v_add_f32_e32 v53, v50, v51
	v_add_f32_e32 v50, v53, v54
	v_add_f32_e32 v53, v50, v55
	v_add_f32_e32 v50, v53, v56
	v_add_f32_e32 v53, v50, v57
	v_add_f32_e32 v50, v53, v58
	v_add_f32_e32 v50, v50, v59
	s_nop 1
	v_max_f32_dpp v51, v50, v50 quad_perm:[1,0,3,2] row_mask:0xf bank_mask:0xf
	s_nop 1
	v_max_f32_dpp v51, v51, v51 quad_perm:[2,3,0,1] row_mask:0xf bank_mask:0xf
	s_nop 1
	v_max_f32_dpp v51, v51, v51 row_half_mirror row_mask:0xf bank_mask:0xf
	s_nop 1
	v_max_f32_dpp v51, v51, v51 row_mirror row_mask:0xf bank_mask:0xf
	v_sub_f32_e32 v50, v50, v51
	v_mul_f32_e32 v50, 0x3fb8aa3b, v50
	v_exp_f32_e32 v50, v50
	s_nop 1
	v_add_f32_dpp v51, v50, v50 quad_perm:[1,0,3,2] row_mask:0xf bank_mask:0xf
	s_nop 1
	v_add_f32_dpp v51, v51, v51 quad_perm:[2,3,0,1] row_mask:0xf bank_mask:0xf
	s_nop 1
	v_add_f32_dpp v51, v51, v51 row_half_mirror row_mask:0xf bank_mask:0xf
	s_nop 1
	v_add_f32_dpp v51, v51, v51 row_mirror row_mask:0xf bank_mask:0xf
	v_div_scale_f32 v52, s[8:9], v51, v51, v50
	v_rcp_f32_e32 v53, v52
	s_nop 0
	v_fma_f32 v54, -v52, v53, 1.0
	v_fmac_f32_e32 v53, v54, v53
	v_div_scale_f32 v54, vcc, v50, v51, v50
	v_mul_f32_e32 v55, v54, v53
	v_fma_f32 v56, -v52, v55, v54
	v_fmac_f32_e32 v55, v56, v53
	v_fma_f32 v52, -v52, v55, v54
	v_div_fmas_f32 v52, v52, v53, v55
	v_div_fixup_f32 v52, v52, v51, v50
	v_lshlrev_b64 v[50:51], 6, v[138:139]
	v_lshl_add_u64 v[50:51], v[88:89], 0, v[50:51]
	global_store_dword v[50:51], v52, off
